# read-back / compaction sized by the variant (12/16/20 entries), descent count pass skipped when a candidate was accepted (on top of v60)
# speedup vs baseline: 1.0069x; 1.0035x over previous
.LBB0_777:
	s_mov_b64 s[0:1], 0
	s_cbranch_execz .LBB0_921
	s_waitcnt lgkmcnt(0)
	v_cmp_lt_u32_e32 vcc, 12, v91
	v_cmp_lt_u32_e64 s[0:1], 16, v91
	s_cmp_lg_u64 vcc, 0
	s_cselect_b32 s8, 16, 12
	s_cmp_lg_u64 s[0:1], 0
	s_cselect_b32 s8, 20, s8
	ds_read2st64_b32 v[14:15], v79 offset0:0 offset1:1
	ds_read2st64_b32 v[16:17], v79 offset0:2 offset1:3
	ds_read2st64_b32 v[18:19], v79 offset0:4 offset1:5
	ds_read2st64_b32 v[20:21], v79 offset0:6 offset1:7
	ds_read2st64_b32 v[22:23], v79 offset0:8 offset1:9
	ds_read2st64_b32 v[24:25], v79 offset0:10 offset1:11
	s_cmp_lt_u32 s8, 13
	s_cbranch_scc1 .Lrb12
	ds_read2st64_b32 v[26:27], v79 offset0:12 offset1:13
	ds_read2st64_b32 v[28:29], v79 offset0:14 offset1:15
	s_cmp_lt_u32 s8, 17
	s_cbranch_scc1 .Lrb16
	ds_read2st64_b32 v[30:31], v79 offset0:16 offset1:17
	ds_read2st64_b32 v[32:33], v79 offset0:18 offset1:19
	s_waitcnt lgkmcnt(0)
	v_cmp_lt_u32_e32 vcc, 16, v91
	v_cmp_lt_u32_e64 s[0:1], 17, v91
	v_sub_u32_e32 v30, v30, v11
	v_sub_u32_e32 v31, v31, v11
	v_cndmask_b32_e32 v6, 0, v30, vcc
	v_cndmask_b32_e64 v3, 0, v31, s[0:1]
	v_cmp_lt_u32_e32 vcc, 18, v91
	v_cmp_lt_u32_e64 s[0:1], 19, v91
	v_sub_u32_e32 v32, v32, v11
	v_sub_u32_e32 v33, v33, v11
	v_cndmask_b32_e32 v4, 0, v32, vcc
	v_cndmask_b32_e64 v2, 0, v33, s[0:1]
.Lrb16:
	s_waitcnt lgkmcnt(0)
	v_cmp_lt_u32_e32 vcc, 12, v91
	v_cmp_lt_u32_e64 s[0:1], 13, v91
	v_sub_u32_e32 v26, v26, v11
	v_sub_u32_e32 v27, v27, v11
	v_cndmask_b32_e32 v78, 0, v26, vcc
	v_cndmask_b32_e64 v7, 0, v27, s[0:1]
	v_cmp_lt_u32_e32 vcc, 14, v91
	v_cmp_lt_u32_e64 s[0:1], 15, v91
	v_sub_u32_e32 v28, v28, v11
	v_sub_u32_e32 v29, v29, v11
	v_cndmask_b32_e32 v8, 0, v28, vcc
	v_cndmask_b32_e64 v5, 0, v29, s[0:1]
.Lrb12:
	s_waitcnt lgkmcnt(5)
	v_cmp_lt_u32_e32 vcc, 0, v91
	v_cmp_lt_u32_e64 s[0:1], 1, v91
	v_sub_u32_e32 v14, v14, v11
	v_sub_u32_e32 v15, v15, v11
	v_cndmask_b32_e32 v90, 0, v14, vcc
	v_cndmask_b32_e64 v88, 0, v15, s[0:1]
	s_waitcnt lgkmcnt(4)
	v_cmp_lt_u32_e32 vcc, 2, v91
	v_cmp_lt_u32_e64 s[0:1], 3, v91
	v_sub_u32_e32 v16, v16, v11
	v_sub_u32_e32 v17, v17, v11
	v_cndmask_b32_e32 v89, 0, v16, vcc
	v_cndmask_b32_e64 v86, 0, v17, s[0:1]
	s_waitcnt lgkmcnt(3)
	v_cmp_lt_u32_e32 vcc, 4, v91
	v_cmp_lt_u32_e64 s[0:1], 5, v91
	v_sub_u32_e32 v18, v18, v11
	v_sub_u32_e32 v19, v19, v11
	v_cndmask_b32_e32 v87, 0, v18, vcc
	v_cndmask_b32_e64 v84, 0, v19, s[0:1]
	s_waitcnt lgkmcnt(2)
	v_cmp_lt_u32_e32 vcc, 6, v91
	v_cmp_lt_u32_e64 s[0:1], 7, v91
	v_sub_u32_e32 v20, v20, v11
	v_sub_u32_e32 v21, v21, v11
	v_cndmask_b32_e32 v85, 0, v20, vcc
	v_cndmask_b32_e64 v82, 0, v21, s[0:1]
	s_waitcnt lgkmcnt(1)
	v_cmp_lt_u32_e32 vcc, 8, v91
	v_cmp_lt_u32_e64 s[0:1], 9, v91
	v_sub_u32_e32 v22, v22, v11
	v_sub_u32_e32 v23, v23, v11
	v_cndmask_b32_e32 v83, 0, v22, vcc
	v_cndmask_b32_e64 v80, 0, v23, s[0:1]
	s_waitcnt lgkmcnt(0)
	v_cmp_lt_u32_e32 vcc, 10, v91
	v_cmp_lt_u32_e64 s[0:1], 11, v91
	v_sub_u32_e32 v24, v24, v11
	v_sub_u32_e32 v25, v25, v11
	v_cndmask_b32_e32 v81, 0, v24, vcc
	v_cndmask_b32_e64 v9, 0, v25, s[0:1]
	s_lshl_b32 s10, s94, 23
	s_cmp_gt_u32 s8, 12
	s_mov_b64 s[0:1], -1
	s_cbranch_scc0 .LBB0_873
	s_cmp_lt_u32 s8, 17
	s_cbranch_scc1 .LBB0_826
	s_mov_b32 s0, 23
	s_mov_b32 s9, s10
.LBB0_821:
	s_add_i32 s0, s0, -1
	s_lshl_b32 s1, 1, s0
	s_or_b32 s1, s1, s9
	s_waitcnt lgkmcnt(0)
	v_cmp_le_u32_e64 s[14:15], s1, v90
	v_cmp_le_u32_e64 s[16:17], s1, v88
	v_cmp_le_u32_e64 s[18:19], s1, v89
	v_cmp_le_u32_e64 s[20:21], s1, v86
	v_cmp_le_u32_e64 s[22:23], s1, v87
	v_cmp_le_u32_e64 s[24:25], s1, v84
	v_cmp_le_u32_e64 s[26:27], s1, v85
	v_cmp_le_u32_e64 s[28:29], s1, v82
	v_cmp_le_u32_e64 s[30:31], s1, v83
	v_cmp_le_u32_e64 s[34:35], s1, v80
	v_cmp_le_u32_e64 s[36:37], s1, v81
	v_cmp_le_u32_e64 s[38:39], s1, v9
	s_bcnt1_i32_b64 s11, s[14:15]
	s_bcnt1_i32_b64 s12, s[16:17]
	s_add_i32 s11, s11, s12
	s_bcnt1_i32_b64 s12, s[18:19]
	s_add_i32 s11, s11, s12
	s_bcnt1_i32_b64 s12, s[20:21]
	s_add_i32 s11, s11, s12
	s_bcnt1_i32_b64 s12, s[22:23]
	s_add_i32 s11, s11, s12
	s_bcnt1_i32_b64 s12, s[24:25]
	s_add_i32 s11, s11, s12
	v_cmp_le_u32_e64 s[14:15], s1, v78
	v_cmp_le_u32_e64 s[16:17], s1, v7
	v_cmp_le_u32_e64 s[18:19], s1, v8
	v_cmp_le_u32_e64 s[20:21], s1, v5
	v_cmp_le_u32_e64 s[22:23], s1, v6
	v_cmp_le_u32_e64 s[24:25], s1, v3
	s_bcnt1_i32_b64 s12, s[26:27]
	s_add_i32 s11, s11, s12
	s_bcnt1_i32_b64 s12, s[28:29]
	s_add_i32 s11, s11, s12
	s_bcnt1_i32_b64 s12, s[30:31]
	s_add_i32 s11, s11, s12
	s_bcnt1_i32_b64 s12, s[34:35]
	s_add_i32 s11, s11, s12
	s_bcnt1_i32_b64 s12, s[36:37]
	s_add_i32 s11, s11, s12
	s_bcnt1_i32_b64 s12, s[38:39]
	s_add_i32 s11, s11, s12
	v_cmp_le_u32_e64 s[26:27], s1, v4
	v_cmp_le_u32_e64 s[28:29], s1, v2
	s_bcnt1_i32_b64 s12, s[14:15]
	s_add_i32 s11, s11, s12
	s_bcnt1_i32_b64 s12, s[16:17]
	s_add_i32 s11, s11, s12
	s_bcnt1_i32_b64 s12, s[18:19]
	s_add_i32 s11, s11, s12
	s_bcnt1_i32_b64 s12, s[20:21]
	s_add_i32 s11, s11, s12
	s_bcnt1_i32_b64 s12, s[22:23]
	s_add_i32 s11, s11, s12
	s_bcnt1_i32_b64 s12, s[24:25]
	s_add_i32 s11, s11, s12
	s_bcnt1_i32_b64 s12, s[26:27]
	s_add_i32 s11, s11, s12
	s_bcnt1_i32_b64 s12, s[28:29]
	s_add_i32 s11, s11, s12
	s_cmpk_gt_u32 s11, 0xff
	s_cselect_b32 s9, s1, s9
	s_cmpk_eq_i32 s11, 0x100
	s_cbranch_scc1 .LBB0_825
	s_cmp_lt_u32 s0, 17
	s_cbranch_scc0 .LBB0_821
	s_cmp_lg_u32 s9, s10
	s_cbranch_scc1 .Ltiewalk_822
	v_cmp_le_u32_e64 s[14:15], s9, v90
	v_cmp_le_u32_e64 s[16:17], s9, v88
	v_cmp_le_u32_e64 s[18:19], s9, v89
	v_cmp_le_u32_e64 s[20:21], s9, v86
	v_cmp_le_u32_e64 s[22:23], s9, v87
	v_cmp_le_u32_e64 s[24:25], s9, v84
	v_cmp_le_u32_e64 s[26:27], s9, v85
	v_cmp_le_u32_e64 s[28:29], s9, v82
	v_cmp_le_u32_e64 s[30:31], s9, v83
	v_cmp_le_u32_e64 s[34:35], s9, v80
	v_cmp_le_u32_e64 s[36:37], s9, v81
	v_cmp_le_u32_e64 s[38:39], s9, v9
	s_bcnt1_i32_b64 s0, s[14:15]
	s_bcnt1_i32_b64 s1, s[16:17]
	s_add_i32 s0, s0, s1
	s_bcnt1_i32_b64 s1, s[18:19]
	s_add_i32 s0, s0, s1
	s_bcnt1_i32_b64 s1, s[20:21]
	s_add_i32 s0, s0, s1
	s_bcnt1_i32_b64 s1, s[22:23]
	s_add_i32 s0, s0, s1
	s_bcnt1_i32_b64 s1, s[24:25]
	s_add_i32 s0, s0, s1
	v_cmp_le_u32_e64 s[14:15], s9, v78
	v_cmp_le_u32_e64 s[16:17], s9, v7
	v_cmp_le_u32_e64 s[18:19], s9, v8
	v_cmp_le_u32_e64 s[20:21], s9, v5
	v_cmp_le_u32_e64 s[22:23], s9, v6
	v_cmp_le_u32_e64 s[24:25], s9, v3
	s_bcnt1_i32_b64 s1, s[26:27]
	s_add_i32 s0, s0, s1
	s_bcnt1_i32_b64 s1, s[28:29]
	s_add_i32 s0, s0, s1
	s_bcnt1_i32_b64 s1, s[30:31]
	s_add_i32 s0, s0, s1
	s_bcnt1_i32_b64 s1, s[34:35]
	s_add_i32 s0, s0, s1
	s_bcnt1_i32_b64 s1, s[36:37]
	s_add_i32 s0, s0, s1
	s_bcnt1_i32_b64 s1, s[38:39]
	s_add_i32 s0, s0, s1
	v_cmp_le_u32_e64 s[26:27], s9, v4
	v_cmp_le_u32_e64 s[28:29], s9, v2
	s_bcnt1_i32_b64 s1, s[14:15]
	s_add_i32 s0, s0, s1
	s_bcnt1_i32_b64 s1, s[16:17]
	s_add_i32 s0, s0, s1
	s_bcnt1_i32_b64 s1, s[18:19]
	s_add_i32 s0, s0, s1
	s_bcnt1_i32_b64 s1, s[20:21]
	s_add_i32 s0, s0, s1
	s_bcnt1_i32_b64 s1, s[22:23]
	s_add_i32 s0, s0, s1
	s_bcnt1_i32_b64 s1, s[24:25]
	s_add_i32 s0, s0, s1
	s_bcnt1_i32_b64 s1, s[26:27]
	s_add_i32 s0, s0, s1
	s_bcnt1_i32_b64 s1, s[28:29]
	s_add_i32 s0, s0, s1
	s_cmpk_eq_i32 s0, 0x100
	s_cbranch_scc1 .LBB0_825
.Ltiewalk_822:
	s_or_b32 s9, s9, 0xe000
	s_mov_b32 s0, 12

.LBB0_828:
	s_add_i32 s0, s0, -1
	s_lshl_b32 s1, 1, s0
	s_or_b32 s1, s1, s9
	s_waitcnt lgkmcnt(0)
	v_cmp_le_u32_e64 s[14:15], s1, v90
	v_cmp_le_u32_e64 s[16:17], s1, v88
	v_cmp_le_u32_e64 s[18:19], s1, v89
	v_cmp_le_u32_e64 s[20:21], s1, v86
	v_cmp_le_u32_e64 s[22:23], s1, v87
	v_cmp_le_u32_e64 s[24:25], s1, v84
	v_cmp_le_u32_e64 s[26:27], s1, v85
	v_cmp_le_u32_e64 s[28:29], s1, v82
	v_cmp_le_u32_e64 s[30:31], s1, v83
	v_cmp_le_u32_e64 s[34:35], s1, v80
	v_cmp_le_u32_e64 s[36:37], s1, v81
	v_cmp_le_u32_e64 s[38:39], s1, v9
	s_bcnt1_i32_b64 s11, s[14:15]
	s_bcnt1_i32_b64 s12, s[16:17]
	s_add_i32 s11, s11, s12
	s_bcnt1_i32_b64 s12, s[18:19]
	s_add_i32 s11, s11, s12
	s_bcnt1_i32_b64 s12, s[20:21]
	s_add_i32 s11, s11, s12
	s_bcnt1_i32_b64 s12, s[22:23]
	s_add_i32 s11, s11, s12
	s_bcnt1_i32_b64 s12, s[24:25]
	s_add_i32 s11, s11, s12
	v_cmp_le_u32_e64 s[14:15], s1, v78
	v_cmp_le_u32_e64 s[16:17], s1, v7
	v_cmp_le_u32_e64 s[18:19], s1, v8
	v_cmp_le_u32_e64 s[20:21], s1, v5
	s_bcnt1_i32_b64 s12, s[26:27]
	s_add_i32 s11, s11, s12
	s_bcnt1_i32_b64 s12, s[28:29]
	s_add_i32 s11, s11, s12
	s_bcnt1_i32_b64 s12, s[30:31]
	s_add_i32 s11, s11, s12
	s_bcnt1_i32_b64 s12, s[34:35]
	s_add_i32 s11, s11, s12
	s_bcnt1_i32_b64 s12, s[36:37]
	s_add_i32 s11, s11, s12
	s_bcnt1_i32_b64 s12, s[38:39]
	s_add_i32 s11, s11, s12
	s_bcnt1_i32_b64 s12, s[14:15]
	s_add_i32 s11, s11, s12
	s_bcnt1_i32_b64 s12, s[16:17]
	s_add_i32 s11, s11, s12
	s_bcnt1_i32_b64 s12, s[18:19]
	s_add_i32 s11, s11, s12
	s_bcnt1_i32_b64 s12, s[20:21]
	s_add_i32 s11, s11, s12
	s_cmpk_gt_u32 s11, 0xff
	s_cselect_b32 s9, s1, s9
	s_cmpk_eq_i32 s11, 0x100
	s_cbranch_scc1 .LBB0_832
	s_cmp_lt_u32 s0, 17
	s_cbranch_scc0 .LBB0_828
	s_cmp_lg_u32 s9, s10
	s_cbranch_scc1 .Ltiewalk_829
	v_cmp_le_u32_e64 s[14:15], s9, v90
	v_cmp_le_u32_e64 s[16:17], s9, v88
	v_cmp_le_u32_e64 s[18:19], s9, v89
	v_cmp_le_u32_e64 s[20:21], s9, v86
	v_cmp_le_u32_e64 s[22:23], s9, v87
	v_cmp_le_u32_e64 s[24:25], s9, v84
	v_cmp_le_u32_e64 s[26:27], s9, v85
	v_cmp_le_u32_e64 s[28:29], s9, v82
	v_cmp_le_u32_e64 s[30:31], s9, v83
	v_cmp_le_u32_e64 s[34:35], s9, v80
	v_cmp_le_u32_e64 s[36:37], s9, v81
	v_cmp_le_u32_e64 s[38:39], s9, v9
	s_bcnt1_i32_b64 s0, s[14:15]
	s_bcnt1_i32_b64 s1, s[16:17]
	s_add_i32 s0, s0, s1
	s_bcnt1_i32_b64 s1, s[18:19]
	s_add_i32 s0, s0, s1
	s_bcnt1_i32_b64 s1, s[20:21]
	s_add_i32 s0, s0, s1
	s_bcnt1_i32_b64 s1, s[22:23]
	s_add_i32 s0, s0, s1
	s_bcnt1_i32_b64 s1, s[24:25]
	s_add_i32 s0, s0, s1
	v_cmp_le_u32_e64 s[14:15], s9, v78
	v_cmp_le_u32_e64 s[16:17], s9, v7
	v_cmp_le_u32_e64 s[18:19], s9, v8
	v_cmp_le_u32_e64 s[20:21], s9, v5
	s_bcnt1_i32_b64 s1, s[26:27]
	s_add_i32 s0, s0, s1
	s_bcnt1_i32_b64 s1, s[28:29]
	s_add_i32 s0, s0, s1
	s_bcnt1_i32_b64 s1, s[30:31]
	s_add_i32 s0, s0, s1
	s_bcnt1_i32_b64 s1, s[34:35]
	s_add_i32 s0, s0, s1
	s_bcnt1_i32_b64 s1, s[36:37]
	s_add_i32 s0, s0, s1
	s_bcnt1_i32_b64 s1, s[38:39]
	s_add_i32 s0, s0, s1
	s_bcnt1_i32_b64 s1, s[14:15]
	s_add_i32 s0, s0, s1
	s_bcnt1_i32_b64 s1, s[16:17]
	s_add_i32 s0, s0, s1
	s_bcnt1_i32_b64 s1, s[18:19]
	s_add_i32 s0, s0, s1
	s_bcnt1_i32_b64 s1, s[20:21]
	s_add_i32 s0, s0, s1
	s_cmpk_eq_i32 s0, 0x100
	s_cbranch_scc1 .LBB0_832

.LBB0_833:
	s_mov_b64 s[12:13], exec
	s_mov_b32 s10, 0
	v_cmp_le_u32_e64 s[14:15], s9, v90
	v_cmp_le_u32_e64 s[16:17], s9, v88
	v_cmp_le_u32_e64 s[18:19], s9, v89
	v_cmp_le_u32_e64 s[20:21], s9, v86
	v_cmp_le_u32_e64 s[22:23], s9, v87
	v_cmp_le_u32_e64 s[24:25], s9, v84
	v_cmp_le_u32_e64 s[26:27], s9, v85
	v_cmp_le_u32_e64 s[28:29], s9, v82
	v_cmp_le_u32_e64 s[30:31], s9, v83
	v_cmp_le_u32_e64 s[34:35], s9, v80
	v_cmp_le_u32_e64 s[36:37], s9, v81
	v_cmp_le_u32_e64 s[38:39], s9, v9
	s_bcnt1_i32_b64 s40, s[14:15]
	s_bcnt1_i32_b64 s41, s[16:17]
	s_bcnt1_i32_b64 s42, s[18:19]
	s_bcnt1_i32_b64 s43, s[20:21]
	s_bcnt1_i32_b64 s46, s[22:23]
	s_bcnt1_i32_b64 s47, s[24:25]
	s_add_i32 s0, s10, s40
	s_add_i32 s0, s0, s41
	s_add_i32 s0, s0, s42
	s_add_i32 s0, s0, s43
	s_add_i32 s0, s0, s46
	s_add_i32 s0, s0, s47
	s_cmpk_gt_u32 s0, 0x100
	s_cbranch_scc1 .Lcomp_slow
	s_lshl_b32 s1, s10, 1
	s_add_i32 s1, s1, s95
	s_mov_b64 exec, s[14:15]
	v_mbcnt_lo_u32_b32 v79, s14, 0
	v_mbcnt_hi_u32_b32 v79, s15, v79
	v_lshl_add_u32 v79, v79, 1, s1
	v_xor_b32_e32 v91, -1, v90
	ds_write_b16 v79, v91
	s_add_i32 s10, s10, s40
	s_lshl_b32 s1, s10, 1
	s_add_i32 s1, s1, s95
	s_mov_b64 exec, s[16:17]
	v_mbcnt_lo_u32_b32 v79, s16, 0
	v_mbcnt_hi_u32_b32 v79, s17, v79
	v_lshl_add_u32 v79, v79, 1, s1
	v_xor_b32_e32 v91, -1, v88
	ds_write_b16 v79, v91
	s_add_i32 s10, s10, s41
	s_lshl_b32 s1, s10, 1
	s_add_i32 s1, s1, s95
	s_mov_b64 exec, s[18:19]
	v_mbcnt_lo_u32_b32 v79, s18, 0
	v_mbcnt_hi_u32_b32 v79, s19, v79
	v_lshl_add_u32 v79, v79, 1, s1
	v_xor_b32_e32 v91, -1, v89
	ds_write_b16 v79, v91
	s_add_i32 s10, s10, s42
	s_lshl_b32 s1, s10, 1
	s_add_i32 s1, s1, s95
	s_mov_b64 exec, s[20:21]
	v_mbcnt_lo_u32_b32 v79, s20, 0
	v_mbcnt_hi_u32_b32 v79, s21, v79
	v_lshl_add_u32 v79, v79, 1, s1
	v_xor_b32_e32 v91, -1, v86
	ds_write_b16 v79, v91
	s_add_i32 s10, s10, s43
	s_lshl_b32 s1, s10, 1
	s_add_i32 s1, s1, s95
	s_mov_b64 exec, s[22:23]
	v_mbcnt_lo_u32_b32 v79, s22, 0
	v_mbcnt_hi_u32_b32 v79, s23, v79
	v_lshl_add_u32 v79, v79, 1, s1
	v_xor_b32_e32 v91, -1, v87
	ds_write_b16 v79, v91
	s_add_i32 s10, s10, s46
	s_lshl_b32 s1, s10, 1
	s_add_i32 s1, s1, s95
	s_mov_b64 exec, s[24:25]
	v_mbcnt_lo_u32_b32 v79, s24, 0
	v_mbcnt_hi_u32_b32 v79, s25, v79
	v_lshl_add_u32 v79, v79, 1, s1
	v_xor_b32_e32 v91, -1, v84
	ds_write_b16 v79, v91
	s_add_i32 s10, s10, s47
	s_mov_b64 exec, s[12:13]
	s_bcnt1_i32_b64 s40, s[26:27]
	s_bcnt1_i32_b64 s41, s[28:29]
	s_bcnt1_i32_b64 s42, s[30:31]
	s_bcnt1_i32_b64 s43, s[34:35]
	s_bcnt1_i32_b64 s46, s[36:37]
	s_bcnt1_i32_b64 s47, s[38:39]
	s_add_i32 s0, s10, s40
	s_add_i32 s0, s0, s41
	s_add_i32 s0, s0, s42
	s_add_i32 s0, s0, s43
	s_add_i32 s0, s0, s46
	s_add_i32 s0, s0, s47
	s_cmpk_gt_u32 s0, 0x100
	s_cbranch_scc1 .Lcomp_slow
	s_lshl_b32 s1, s10, 1
	s_add_i32 s1, s1, s95
	s_mov_b64 exec, s[26:27]
	v_mbcnt_lo_u32_b32 v79, s26, 0
	v_mbcnt_hi_u32_b32 v79, s27, v79
	v_lshl_add_u32 v79, v79, 1, s1
	v_xor_b32_e32 v91, -1, v85
	ds_write_b16 v79, v91
	s_add_i32 s10, s10, s40
	s_lshl_b32 s1, s10, 1
	s_add_i32 s1, s1, s95
	s_mov_b64 exec, s[28:29]
	v_mbcnt_lo_u32_b32 v79, s28, 0
	v_mbcnt_hi_u32_b32 v79, s29, v79
	v_lshl_add_u32 v79, v79, 1, s1
	v_xor_b32_e32 v91, -1, v82
	ds_write_b16 v79, v91
	s_add_i32 s10, s10, s41
	s_lshl_b32 s1, s10, 1
	s_add_i32 s1, s1, s95
	s_mov_b64 exec, s[30:31]
	v_mbcnt_lo_u32_b32 v79, s30, 0
	v_mbcnt_hi_u32_b32 v79, s31, v79
	v_lshl_add_u32 v79, v79, 1, s1
	v_xor_b32_e32 v91, -1, v83
	ds_write_b16 v79, v91
	s_add_i32 s10, s10, s42
	s_lshl_b32 s1, s10, 1
	s_add_i32 s1, s1, s95
	s_mov_b64 exec, s[34:35]
	v_mbcnt_lo_u32_b32 v79, s34, 0
	v_mbcnt_hi_u32_b32 v79, s35, v79
	v_lshl_add_u32 v79, v79, 1, s1
	v_xor_b32_e32 v91, -1, v80
	ds_write_b16 v79, v91
	s_add_i32 s10, s10, s43
	s_lshl_b32 s1, s10, 1
	s_add_i32 s1, s1, s95
	s_mov_b64 exec, s[36:37]
	v_mbcnt_lo_u32_b32 v79, s36, 0
	v_mbcnt_hi_u32_b32 v79, s37, v79
	v_lshl_add_u32 v79, v79, 1, s1
	v_xor_b32_e32 v91, -1, v81
	ds_write_b16 v79, v91
	s_add_i32 s10, s10, s46
	s_lshl_b32 s1, s10, 1
	s_add_i32 s1, s1, s95
	s_mov_b64 exec, s[38:39]
	v_mbcnt_lo_u32_b32 v79, s38, 0
	v_mbcnt_hi_u32_b32 v79, s39, v79
	v_lshl_add_u32 v79, v79, 1, s1
	v_xor_b32_e32 v91, -1, v9
	ds_write_b16 v79, v91
	s_add_i32 s10, s10, s47
	s_mov_b64 exec, s[12:13]
	s_cmp_lt_u32 s8, 13
	s_cbranch_scc1 .LBB0_920
	v_cmp_le_u32_e64 s[14:15], s9, v78
	v_cmp_le_u32_e64 s[16:17], s9, v7
	v_cmp_le_u32_e64 s[18:19], s9, v8
	v_cmp_le_u32_e64 s[20:21], s9, v5
	v_cmp_le_u32_e64 s[26:27], s9, v6
	v_cmp_le_u32_e64 s[28:29], s9, v3
	v_cmp_le_u32_e64 s[30:31], s9, v4
	v_cmp_le_u32_e64 s[34:35], s9, v2
	s_bcnt1_i32_b64 s40, s[14:15]
	s_bcnt1_i32_b64 s41, s[16:17]
	s_bcnt1_i32_b64 s42, s[18:19]
	s_bcnt1_i32_b64 s43, s[20:21]
	s_add_i32 s0, s10, s40
	s_add_i32 s0, s0, s41
	s_add_i32 s0, s0, s42
	s_add_i32 s0, s0, s43
	s_cmpk_gt_u32 s0, 0x100
	s_cbranch_scc1 .Lcomp_slow
	s_lshl_b32 s1, s10, 1
	s_add_i32 s1, s1, s95
	s_mov_b64 exec, s[14:15]
	v_mbcnt_lo_u32_b32 v79, s14, 0
	v_mbcnt_hi_u32_b32 v79, s15, v79
	v_lshl_add_u32 v79, v79, 1, s1
	v_xor_b32_e32 v91, -1, v78
	ds_write_b16 v79, v91
	s_add_i32 s10, s10, s40
	s_lshl_b32 s1, s10, 1
	s_add_i32 s1, s1, s95
	s_mov_b64 exec, s[16:17]
	v_mbcnt_lo_u32_b32 v79, s16, 0
	v_mbcnt_hi_u32_b32 v79, s17, v79
	v_lshl_add_u32 v79, v79, 1, s1
	v_xor_b32_e32 v91, -1, v7
	ds_write_b16 v79, v91
	s_add_i32 s10, s10, s41
	s_lshl_b32 s1, s10, 1
	s_add_i32 s1, s1, s95
	s_mov_b64 exec, s[18:19]
	v_mbcnt_lo_u32_b32 v79, s18, 0
	v_mbcnt_hi_u32_b32 v79, s19, v79
	v_lshl_add_u32 v79, v79, 1, s1
	v_xor_b32_e32 v91, -1, v8
	ds_write_b16 v79, v91
	s_add_i32 s10, s10, s42
	s_lshl_b32 s1, s10, 1
	s_add_i32 s1, s1, s95
	s_mov_b64 exec, s[20:21]
	v_mbcnt_lo_u32_b32 v79, s20, 0
	v_mbcnt_hi_u32_b32 v79, s21, v79
	v_lshl_add_u32 v79, v79, 1, s1
	v_xor_b32_e32 v91, -1, v5
	ds_write_b16 v79, v91
	s_add_i32 s10, s10, s43
	s_mov_b64 exec, s[12:13]
	s_cmp_lt_u32 s8, 17
	s_cbranch_scc1 .LBB0_920
	s_bcnt1_i32_b64 s40, s[26:27]
	s_bcnt1_i32_b64 s41, s[28:29]
	s_bcnt1_i32_b64 s42, s[30:31]
	s_bcnt1_i32_b64 s43, s[34:35]
	s_add_i32 s0, s10, s40
	s_add_i32 s0, s0, s41
	s_add_i32 s0, s0, s42
	s_add_i32 s0, s0, s43
	s_cmpk_gt_u32 s0, 0x100
	s_cbranch_scc1 .Lcomp_slow
	s_lshl_b32 s1, s10, 1
	s_add_i32 s1, s1, s95
	s_mov_b64 exec, s[26:27]
	v_mbcnt_lo_u32_b32 v79, s26, 0
	v_mbcnt_hi_u32_b32 v79, s27, v79
	v_lshl_add_u32 v79, v79, 1, s1
	v_xor_b32_e32 v91, -1, v6
	ds_write_b16 v79, v91
	s_add_i32 s10, s10, s40
	s_lshl_b32 s1, s10, 1
	s_add_i32 s1, s1, s95
	s_mov_b64 exec, s[28:29]
	v_mbcnt_lo_u32_b32 v79, s28, 0
	v_mbcnt_hi_u32_b32 v79, s29, v79
	v_lshl_add_u32 v79, v79, 1, s1
	v_xor_b32_e32 v91, -1, v3
	ds_write_b16 v79, v91
	s_add_i32 s10, s10, s41
	s_lshl_b32 s1, s10, 1
	s_add_i32 s1, s1, s95
	s_mov_b64 exec, s[30:31]
	v_mbcnt_lo_u32_b32 v79, s30, 0
	v_mbcnt_hi_u32_b32 v79, s31, v79
	v_lshl_add_u32 v79, v79, 1, s1
	v_xor_b32_e32 v91, -1, v4
	ds_write_b16 v79, v91
	s_add_i32 s10, s10, s42
	s_lshl_b32 s1, s10, 1
	s_add_i32 s1, s1, s95
	s_mov_b64 exec, s[34:35]
	v_mbcnt_lo_u32_b32 v79, s34, 0
	v_mbcnt_hi_u32_b32 v79, s35, v79
	v_lshl_add_u32 v79, v79, 1, s1
	v_xor_b32_e32 v91, -1, v2
	ds_write_b16 v79, v91
	s_add_i32 s10, s10, s43
	s_mov_b64 exec, s[12:13]
	s_branch .LBB0_920

.LBB0_875:
	s_add_i32 s0, s0, -1
	s_lshl_b32 s1, 1, s0
	s_or_b32 s1, s1, s10
	s_waitcnt lgkmcnt(0)
	v_cmp_le_u32_e64 s[14:15], s1, v90
	v_cmp_le_u32_e64 s[16:17], s1, v88
	v_cmp_le_u32_e64 s[18:19], s1, v89
	v_cmp_le_u32_e64 s[20:21], s1, v86
	v_cmp_le_u32_e64 s[22:23], s1, v87
	v_cmp_le_u32_e64 s[24:25], s1, v84
	v_cmp_le_u32_e64 s[26:27], s1, v85
	v_cmp_le_u32_e64 s[28:29], s1, v82
	v_cmp_le_u32_e64 s[30:31], s1, v83
	v_cmp_le_u32_e64 s[34:35], s1, v80
	v_cmp_le_u32_e64 s[36:37], s1, v81
	v_cmp_le_u32_e64 s[38:39], s1, v9
	s_bcnt1_i32_b64 s9, s[14:15]
	s_bcnt1_i32_b64 s11, s[16:17]
	s_add_i32 s9, s9, s11
	s_bcnt1_i32_b64 s11, s[18:19]
	s_add_i32 s9, s9, s11
	s_bcnt1_i32_b64 s11, s[20:21]
	s_add_i32 s9, s9, s11
	s_bcnt1_i32_b64 s11, s[22:23]
	s_add_i32 s9, s9, s11
	s_bcnt1_i32_b64 s11, s[24:25]
	s_add_i32 s9, s9, s11
	s_bcnt1_i32_b64 s11, s[26:27]
	s_add_i32 s9, s9, s11
	s_bcnt1_i32_b64 s11, s[28:29]
	s_add_i32 s9, s9, s11
	s_bcnt1_i32_b64 s11, s[30:31]
	s_add_i32 s9, s9, s11
	s_bcnt1_i32_b64 s11, s[34:35]
	s_add_i32 s9, s9, s11
	s_bcnt1_i32_b64 s11, s[36:37]
	s_add_i32 s9, s9, s11
	s_bcnt1_i32_b64 s11, s[38:39]
	s_add_i32 s9, s9, s11
	s_cmpk_gt_u32 s9, 0xff
	s_cselect_b32 s10, s1, s10
	s_cmpk_eq_i32 s9, 0x100
	s_cbranch_scc1 .LBB0_879
	s_cmp_lt_u32 s0, 17
	s_cbranch_scc0 .LBB0_875
	s_lshl_b32 s1, s94, 23
	s_cmp_lg_u32 s10, s1
	s_cbranch_scc1 .Ltiewalk_876
	v_cmp_le_u32_e64 s[14:15], s10, v90
	v_cmp_le_u32_e64 s[16:17], s10, v88
	v_cmp_le_u32_e64 s[18:19], s10, v89
	v_cmp_le_u32_e64 s[20:21], s10, v86
	v_cmp_le_u32_e64 s[22:23], s10, v87
	v_cmp_le_u32_e64 s[24:25], s10, v84
	v_cmp_le_u32_e64 s[26:27], s10, v85
	v_cmp_le_u32_e64 s[28:29], s10, v82
	v_cmp_le_u32_e64 s[30:31], s10, v83
	v_cmp_le_u32_e64 s[34:35], s10, v80
	v_cmp_le_u32_e64 s[36:37], s10, v81
	v_cmp_le_u32_e64 s[38:39], s10, v9
	s_bcnt1_i32_b64 s0, s[14:15]
	s_bcnt1_i32_b64 s1, s[16:17]
	s_add_i32 s0, s0, s1
	s_bcnt1_i32_b64 s1, s[18:19]
	s_add_i32 s0, s0, s1
	s_bcnt1_i32_b64 s1, s[20:21]
	s_add_i32 s0, s0, s1
	s_bcnt1_i32_b64 s1, s[22:23]
	s_add_i32 s0, s0, s1
	s_bcnt1_i32_b64 s1, s[24:25]
	s_add_i32 s0, s0, s1
	s_bcnt1_i32_b64 s1, s[26:27]
	s_add_i32 s0, s0, s1
	s_bcnt1_i32_b64 s1, s[28:29]
	s_add_i32 s0, s0, s1
	s_bcnt1_i32_b64 s1, s[30:31]
	s_add_i32 s0, s0, s1
	s_bcnt1_i32_b64 s1, s[34:35]
	s_add_i32 s0, s0, s1
	s_bcnt1_i32_b64 s1, s[36:37]
	s_add_i32 s0, s0, s1
	s_bcnt1_i32_b64 s1, s[38:39]
	s_add_i32 s0, s0, s1
	s_cmpk_eq_i32 s0, 0x100
	s_cbranch_scc1 .LBB0_879
.Ltiewalk_876:
	s_or_b32 s10, s10, 0xe000
	s_mov_b32 s0, 12
